# baseline (speedup 1.0000x reference)
_Z7k_finalPKfS0_S0_Pf:
	s_load_dwordx8 s[4:11], s[0:1], 0x0
	s_lshl_b32 s2, s2, 4
	v_lshrrev_b32_e32 v1, 3, v0
	v_or_b32_e32 v34, s2, v1
	v_bfe_u32 v1, v0, 2, 1
	s_ashr_i32 s0, s2, 3
	v_bfe_u32 v35, v0, 1, 1
	s_and_b32 s0, s0, -4
	v_lshlrev_b32_e32 v2, 1, v1
	v_lshlrev_b32_e32 v3, 4, v34
	v_and_b32_e32 v50, 1, v0
	v_or3_b32 v2, s0, v2, v35
	v_and_b32_e32 v3, 0x1f0, v3
	v_lshl_or_b32 v36, v50, 9, v3
	v_mov_b32_e32 v37, 0
	v_ashrrev_i32_e32 v3, 31, v2
	s_waitcnt lgkmcnt(0)
	v_lshl_add_u64 v[4:5], s[4:5], 0, v[36:37]
	v_lshlrev_b64 v[2:3], 10, v[2:3]
	v_lshl_add_u64 v[30:31], v[4:5], 0, v[2:3]
	s_mov_b32 s0, 0x80000
	v_add_co_u32_e32 v6, vcc, s0, v30
	s_mov_b32 s0, 0x100000
	s_nop 0
	v_addc_co_u32_e32 v7, vcc, 0, v31, vcc
	v_add_co_u32_e32 v14, vcc, s0, v30
	s_mov_b32 s0, 0x180000
	s_nop 0
	v_addc_co_u32_e32 v15, vcc, 0, v31, vcc
	v_add_co_u32_e32 v16, vcc, s0, v30
	s_mov_b32 s0, 0x200000
	s_nop 0
	v_addc_co_u32_e32 v17, vcc, 0, v31, vcc
	global_load_dwordx4 v[22:25], v[30:31], off
	global_load_dwordx4 v[2:5], v[6:7], off
	global_load_dwordx4 v[10:13], v[14:15], off
	s_nop 0
	global_load_dwordx4 v[6:9], v[16:17], off
	v_add_co_u32_e32 v26, vcc, s0, v30
	s_mov_b32 s0, 0x280000
	s_nop 0
	v_addc_co_u32_e32 v27, vcc, 0, v31, vcc
	v_add_co_u32_e32 v28, vcc, s0, v30
	s_mov_b32 s0, 0x300000
	s_nop 0
	v_addc_co_u32_e32 v29, vcc, 0, v31, vcc
	global_load_dwordx4 v[18:21], v[26:27], off
	global_load_dwordx4 v[14:17], v[28:29], off
	v_add_co_u32_e32 v26, vcc, s0, v30
	s_mov_b32 s0, 0x380000
	s_nop 0
	v_addc_co_u32_e32 v27, vcc, 0, v31, vcc
	v_add_co_u32_e32 v30, vcc, s0, v30
	global_load_dwordx4 v[26:29], v[26:27], off
	s_nop 0
	v_addc_co_u32_e32 v31, vcc, 0, v31, vcc
	global_load_dwordx4 v[30:33], v[30:31], off
	v_lshlrev_b32_e32 v36, 6, v35
	v_and_or_b32 v44, v0, 15, s2
	v_mov_b32_e32 v45, v37
	v_mov_b32_e32 v49, v37
	v_lshl_or_b32 v1, v1, 7, v36
	v_add_u32_e32 v48, 0x6000, v44
	v_mov_b32_e32 v39, v37
	v_mov_b32_e32 v41, v37
	v_mov_b32_e32 v43, v37
	v_mov_b32_e32 v47, v37
	v_add_u32_e32 v38, 0x1000, v44
	v_add_u32_e32 v40, 0x2000, v44
	v_add_u32_e32 v42, 0x4000, v44
	v_add_u32_e32 v46, 0x5000, v44
	v_lshl_or_b32 v36, v50, 4, v1
	v_lshl_add_u64 v[50:51], v[44:45], 2, s[8:9]
	v_lshl_add_u64 v[48:49], v[48:49], 2, s[8:9]
	v_lshl_add_u64 v[52:53], v[38:39], 2, s[8:9]
	v_lshl_add_u64 v[54:55], v[40:41], 2, s[8:9]
	v_lshl_add_u64 v[56:57], v[42:43], 2, s[8:9]
	v_lshl_add_u64 v[46:47], v[46:47], 2, s[8:9]
	global_load_dword v40, v[50:51], off
	global_load_dword v42, v[52:53], off
	global_load_dword v38, v[54:55], off
	global_load_dword v41, v[56:57], off
	global_load_dword v43, v[46:47], off
	global_load_dword v39, v[48:49], off
	v_ashrrev_i32_e32 v35, 31, v34
	v_lshlrev_b64 v[62:63], 8, v[34:35]
	v_lshl_add_u64 v[62:63], s[6:7], 0, v[62:63]
	v_lshl_add_u64 v[62:63], v[62:63], 0, v[36:37]
	global_load_dwordx4 v[64:67], v[62:63], off
	global_load_dwordx4 v[68:71], v[62:63], off offset:32
	v_add_u32_e32 v72, 0x3000, v44
	v_mov_b32_e32 v73, 0
	v_lshl_add_u64 v[72:73], v[72:73], 2, s[8:9]
	global_load_dword v76, v[72:73], off
	v_add_u32_e32 v74, 0x7000, v44
	v_mov_b32_e32 v75, 0
	v_lshl_add_u64 v[74:75], v[74:75], 2, s[8:9]
	global_load_dword v77, v[74:75], off
	s_mov_b64 s[0:1], 0x8000
	s_waitcnt vmcnt(17)
	v_cvt_f32_f16_e32 v58, v22
	s_waitcnt vmcnt(15)
	v_cvt_f32_f16_e32 v48, v10
	v_cvt_f32_f16_sdwa v49, v10 dst_sel:DWORD dst_unused:UNUSED_PAD src0_sel:WORD_1
	s_waitcnt vmcnt(14)
	v_cvt_f32_f16_e32 v50, v6
	v_cvt_f32_f16_sdwa v51, v6 dst_sel:DWORD dst_unused:UNUSED_PAD src0_sel:WORD_1
	v_cvt_f32_f16_e32 v10, v11
	v_cvt_f32_f16_sdwa v11, v11 dst_sel:DWORD dst_unused:UNUSED_PAD src0_sel:WORD_1
	v_cvt_f32_f16_e32 v6, v7
	v_cvt_f32_f16_sdwa v7, v7 dst_sel:DWORD dst_unused:UNUSED_PAD src0_sel:WORD_1
	v_cvt_f32_f16_sdwa v59, v22 dst_sel:DWORD dst_unused:UNUSED_PAD src0_sel:WORD_1
	v_cvt_f32_f16_e32 v60, v2
	v_cvt_f32_f16_sdwa v61, v2 dst_sel:DWORD dst_unused:UNUSED_PAD src0_sel:WORD_1
	v_cvt_f32_f16_e32 v22, v23
	v_cvt_f32_f16_sdwa v23, v23 dst_sel:DWORD dst_unused:UNUSED_PAD src0_sel:WORD_1
	v_cvt_f32_f16_e32 v2, v3
	v_cvt_f32_f16_sdwa v3, v3 dst_sel:DWORD dst_unused:UNUSED_PAD src0_sel:WORD_1
	s_waitcnt vmcnt(12)
	v_cvt_f32_f16_e32 v54, v14
	v_cvt_f32_f16_sdwa v55, v14 dst_sel:DWORD dst_unused:UNUSED_PAD src0_sel:WORD_1
	v_pk_add_f32 v[6:7], v[10:11], v[6:7]
	v_cvt_f32_f16_e32 v10, v19
	v_cvt_f32_f16_sdwa v11, v19 dst_sel:DWORD dst_unused:UNUSED_PAD src0_sel:WORD_1
	v_cvt_f32_f16_e32 v14, v15
	v_cvt_f32_f16_sdwa v15, v15 dst_sel:DWORD dst_unused:UNUSED_PAD src0_sel:WORD_1
	v_pk_add_f32 v[2:3], v[22:23], v[2:3]
	v_pk_add_f32 v[46:47], v[58:59], v[60:61]
	v_cvt_f32_f16_e32 v52, v18
	v_cvt_f32_f16_sdwa v53, v18 dst_sel:DWORD dst_unused:UNUSED_PAD src0_sel:WORD_1
	s_waitcnt vmcnt(11)
	v_cvt_f32_f16_e32 v56, v26
	v_cvt_f32_f16_sdwa v57, v26 dst_sel:DWORD dst_unused:UNUSED_PAD src0_sel:WORD_1
	s_waitcnt vmcnt(10)
	v_cvt_f32_f16_e32 v58, v30
	v_cvt_f32_f16_sdwa v59, v30 dst_sel:DWORD dst_unused:UNUSED_PAD src0_sel:WORD_1
	v_pk_add_f32 v[2:3], v[2:3], v[6:7]
	v_pk_add_f32 v[6:7], v[10:11], v[14:15]
	v_cvt_f32_f16_e32 v10, v27
	v_cvt_f32_f16_sdwa v11, v27 dst_sel:DWORD dst_unused:UNUSED_PAD src0_sel:WORD_1
	v_cvt_f32_f16_e32 v14, v31
	v_cvt_f32_f16_sdwa v15, v31 dst_sel:DWORD dst_unused:UNUSED_PAD src0_sel:WORD_1
	v_pk_add_f32 v[48:49], v[48:49], v[50:51]
	v_pk_add_f32 v[50:51], v[56:57], v[58:59]
	v_pk_add_f32 v[46:47], v[46:47], v[48:49]
	v_pk_add_f32 v[48:49], v[52:53], v[54:55]
	v_pk_add_f32 v[10:11], v[10:11], v[14:15]
	v_pk_add_f32 v[48:49], v[48:49], v[50:51]
	v_pk_add_f32 v[6:7], v[6:7], v[10:11]
	v_add_u32_e32 v50, 0x3000, v44
	v_add_u32_e32 v22, 0x7000, v44
	v_pk_add_f32 v[44:45], v[46:47], v[48:49]
	v_pk_add_f32 v[46:47], v[2:3], v[6:7]
	v_cvt_f32_f16_e32 v6, v24
	v_cvt_f32_f16_sdwa v7, v24 dst_sel:DWORD dst_unused:UNUSED_PAD src0_sel:WORD_1
	v_cvt_f32_f16_e32 v10, v4
	v_cvt_f32_f16_sdwa v11, v4 dst_sel:DWORD dst_unused:UNUSED_PAD src0_sel:WORD_1
	v_cvt_f32_f16_e32 v14, v12
	v_cvt_f32_f16_sdwa v15, v12 dst_sel:DWORD dst_unused:UNUSED_PAD src0_sel:WORD_1
	v_cvt_f32_f16_e32 v26, v8
	v_cvt_f32_f16_sdwa v27, v8 dst_sel:DWORD dst_unused:UNUSED_PAD src0_sel:WORD_1
	v_pk_add_f32 v[6:7], v[6:7], v[10:11]
	v_mov_b32_e32 v51, v37
	v_lshl_add_u64 v[18:19], v[50:51], 2, s[8:9]
	v_pk_add_f32 v[10:11], v[14:15], v[26:27]
	v_cvt_f32_f16_e32 v14, v16
	v_pk_add_f32 v[10:11], v[6:7], v[10:11]
	v_cvt_f32_f16_e32 v6, v20
	v_cvt_f32_f16_sdwa v7, v20 dst_sel:DWORD dst_unused:UNUSED_PAD src0_sel:WORD_1
	v_cvt_f32_f16_sdwa v15, v16 dst_sel:DWORD dst_unused:UNUSED_PAD src0_sel:WORD_1
	v_mov_b32_e32 v23, v37
	v_lshl_add_u64 v[22:23], v[22:23], 2, s[8:9]
	v_lshlrev_b64 v[18:19], 8, v[34:35]
	v_pk_add_f32 v[14:15], v[6:7], v[14:15]
	v_lshl_add_u64 v[6:7], s[6:7], 0, v[18:19]
	v_cvt_f32_f16_e32 v26, v25
	v_cvt_f32_f16_sdwa v27, v25 dst_sel:DWORD dst_unused:UNUSED_PAD src0_sel:WORD_1
	v_cvt_f32_f16_e32 v22, v28
	v_cvt_f32_f16_sdwa v23, v28 dst_sel:DWORD dst_unused:UNUSED_PAD src0_sel:WORD_1
	v_cvt_f32_f16_e32 v24, v32
	v_cvt_f32_f16_sdwa v25, v32 dst_sel:DWORD dst_unused:UNUSED_PAD src0_sel:WORD_1
	v_lshl_add_u64 v[30:31], v[6:7], 0, v[36:37]
	v_cvt_f32_f16_e32 v48, v5
	v_cvt_f32_f16_sdwa v49, v5 dst_sel:DWORD dst_unused:UNUSED_PAD src0_sel:WORD_1
	v_pk_add_f32 v[22:23], v[22:23], v[24:25]
	v_cvt_f32_f16_e32 v12, v13
	v_pk_add_f32 v[14:15], v[14:15], v[22:23]
	v_cvt_f32_f16_sdwa v13, v13 dst_sel:DWORD dst_unused:UNUSED_PAD src0_sel:WORD_1
	v_cvt_f32_f16_e32 v8, v9
	v_cvt_f32_f16_sdwa v9, v9 dst_sel:DWORD dst_unused:UNUSED_PAD src0_sel:WORD_1
	v_pk_add_f32 v[10:11], v[10:11], v[14:15]
	v_pk_add_f32 v[14:15], v[26:27], v[48:49]
	v_cvt_f32_f16_e32 v20, v21
	v_cvt_f32_f16_sdwa v21, v21 dst_sel:DWORD dst_unused:UNUSED_PAD src0_sel:WORD_1
	v_cvt_f32_f16_e32 v16, v17
	v_cvt_f32_f16_sdwa v17, v17 dst_sel:DWORD dst_unused:UNUSED_PAD src0_sel:WORD_1
	v_cvt_f32_f16_e32 v26, v29
	v_cvt_f32_f16_sdwa v27, v29 dst_sel:DWORD dst_unused:UNUSED_PAD src0_sel:WORD_1
	v_cvt_f32_f16_e32 v28, v33
	v_cvt_f32_f16_sdwa v29, v33 dst_sel:DWORD dst_unused:UNUSED_PAD src0_sel:WORD_1
	v_pk_add_f32 v[8:9], v[12:13], v[8:9]
	v_pk_add_f32 v[12:13], v[20:21], v[16:17]
	v_pk_add_f32 v[8:9], v[14:15], v[8:9]
	v_pk_add_f32 v[14:15], v[26:27], v[28:29]
	v_and_b32_e32 v16, 7, v0
	v_pk_add_f32 v[12:13], v[12:13], v[14:15]
	v_pk_add_f32 v[12:13], v[8:9], v[12:13]
	v_lshl_add_u64 v[78:79], s[10:11], 0, v[18:19]
	v_lshl_add_u64 v[78:79], v[78:79], 0, v[36:37]
	v_lshl_add_u64 v[78:79], v[78:79], 0, s[0:1]
	global_store_dwordx4 v[78:79], v[44:47], off sc1
	global_store_dwordx4 v[78:79], v[10:13], off offset:32 sc1
	s_waitcnt vmcnt(5)
	v_mul_f32_e32 v1, v65, v45
	v_fmac_f32_e32 v1, v64, v44
	v_mbcnt_lo_u32_b32 v4, -1, 0
	v_fmac_f32_e32 v1, v66, v46
	v_mbcnt_hi_u32_b32 v14, -1, v4
	v_fmac_f32_e32 v1, v67, v47
	v_and_b32_e32 v5, 64, v14
	s_waitcnt vmcnt(4)
	v_fmac_f32_e32 v1, v68, v10
	v_xor_b32_e32 v4, 1, v14
	v_add_u32_e32 v15, 64, v5
	v_fmac_f32_e32 v1, v69, v11
	v_cmp_lt_i32_e32 vcc, v4, v15
	v_fmac_f32_e32 v1, v70, v12
	v_fmac_f32_e32 v1, v71, v13
	v_cndmask_b32_e32 v4, v14, v4, vcc
	v_lshlrev_b32_e32 v4, 2, v4
	ds_bpermute_b32 v8, v4, v1
	v_lshl_add_u64 v[4:5], s[10:11], 0, v[18:19]
	v_lshl_add_u64 v[6:7], v[4:5], 0, v[36:37]
	v_xor_b32_e32 v4, 2, v14
	v_cmp_lt_i32_e32 vcc, v4, v15
	s_waitcnt lgkmcnt(0)
	v_add_f32_e32 v1, v1, v8
	v_lshl_add_u64 v[8:9], v[6:7], 0, s[0:1]
	v_cndmask_b32_e32 v4, v14, v4, vcc
	v_lshlrev_b32_e32 v4, 2, v4
	ds_bpermute_b32 v4, v4, v1
	s_mov_b32 s0, 0x8000
	s_waitcnt lgkmcnt(0)
	v_add_f32_e32 v1, v1, v4
	v_xor_b32_e32 v4, 4, v14
	v_cmp_lt_i32_e32 vcc, v4, v15
	s_nop 1
	v_cndmask_b32_e32 v4, v14, v4, vcc
	v_lshlrev_b32_e32 v4, 2, v4
	ds_bpermute_b32 v4, v4, v1
	v_add_co_u32_e32 v6, vcc, s0, v6
	s_nop 1
	v_addc_co_u32_e32 v7, vcc, 0, v7, vcc
	v_cmp_eq_u32_e32 vcc, 0, v16
	s_and_saveexec_b64 s[0:1], vcc
	s_cbranch_execnz .LBB1_3
	s_or_b64 exec, exec, s[0:1]
	v_cmp_gt_u32_e32 vcc, 16, v0
	s_and_saveexec_b64 s[0:1], vcc
	s_cbranch_execnz .LBB1_4

.LBB1_4:
	s_waitcnt vmcnt(2) lgkmcnt(0)
	v_pk_add_f32 v[4:5], v[40:41], v[42:43]
	v_pk_add_f32 v[2:3], v[38:39], v[76:77]
	v_or_b32_e32 v0, s2, v0
	v_pk_add_f32 v[2:3], v[4:5], v[2:3]
	v_mov_b32_e32 v1, 0
	v_add_f32_e32 v2, v2, v3
	v_lshl_add_u64 v[0:1], v[0:1], 2, s[10:11]
	global_store_dword v[0:1], v2, off sc1
	s_endpgm
	s_nop 0
	s_nop 0
	s_nop 0
	s_nop 0
	s_nop 0
	s_nop 0
	s_nop 0
	s_nop 0
	s_nop 0
	s_nop 0
	s_nop 0
	s_nop 0
	s_nop 0
	s_nop 0
	s_nop 0
	s_endpgm

	.amdhsa_kernel _Z7k_finalPKfS0_S0_Pf
		.amdhsa_group_segment_fixed_size 0
		.amdhsa_private_segment_fixed_size 0
		.amdhsa_kernarg_size 32
		.amdhsa_user_sgpr_count 2
		.amdhsa_user_sgpr_dispatch_ptr 0
		.amdhsa_user_sgpr_queue_ptr 0
		.amdhsa_user_sgpr_kernarg_segment_ptr 1
		.amdhsa_user_sgpr_dispatch_id 0
		.amdhsa_user_sgpr_kernarg_preload_length 0
		.amdhsa_user_sgpr_kernarg_preload_offset 0
		.amdhsa_user_sgpr_private_segment_size 0
		.amdhsa_uses_dynamic_stack 0
		.amdhsa_enable_private_segment 0
		.amdhsa_system_sgpr_workgroup_id_x 1
		.amdhsa_system_sgpr_workgroup_id_y 0
		.amdhsa_system_sgpr_workgroup_id_z 0
		.amdhsa_system_sgpr_workgroup_info 0
		.amdhsa_system_vgpr_workitem_id 0
		.amdhsa_next_free_vgpr 82
		.amdhsa_next_free_sgpr 12
		.amdhsa_accum_offset 84
		.amdhsa_reserve_vcc 1
		.amdhsa_float_round_mode_32 0
		.amdhsa_float_round_mode_16_64 0
		.amdhsa_float_denorm_mode_32 3
		.amdhsa_float_denorm_mode_16_64 3
		.amdhsa_dx10_clamp 1
		.amdhsa_ieee_mode 1
		.amdhsa_fp16_overflow 0
		.amdhsa_tg_split 0
		.amdhsa_exception_fp_ieee_invalid_op 0
		.amdhsa_exception_fp_denorm_src 0
		.amdhsa_exception_fp_ieee_div_zero 0
		.amdhsa_exception_fp_ieee_overflow 0
		.amdhsa_exception_fp_ieee_underflow 0
		.amdhsa_exception_fp_ieee_inexact 0
		.amdhsa_exception_int_div_zero 0
	.end_amdhsa_kernel

amdhsa.kernels:
  - .agpr_count:     16
    .args:
      - .actual_access:  read_only
        .address_space:  global
        .offset:         0
        .size:           8
        .value_kind:     global_buffer
      - .actual_access:  read_only
        .address_space:  global
        .offset:         8
        .size:           8
        .value_kind:     global_buffer
      - .actual_access:  read_only
        .address_space:  global
        .offset:         16
        .size:           8
        .value_kind:     global_buffer
      - .actual_access:  read_only
        .address_space:  global
        .offset:         24
        .size:           8
        .value_kind:     global_buffer
      - .actual_access:  write_only
        .address_space:  global
        .offset:         32
        .size:           8
        .value_kind:     global_buffer
      - .actual_access:  write_only
        .address_space:  global
        .offset:         40
        .size:           8
        .value_kind:     global_buffer
      - .actual_access:  write_only
        .address_space:  global
        .offset:         48
        .size:           8
        .value_kind:     global_buffer
      - .actual_access:  write_only
        .address_space:  global
        .offset:         56
        .size:           8
        .value_kind:     global_buffer
      - .actual_access:  read_only
        .address_space:  global
        .offset:         64
        .size:           8
        .value_kind:     global_buffer
      - .actual_access:  read_only
        .address_space:  global
        .offset:         72
        .size:           8
        .value_kind:     global_buffer
      - .actual_access:  read_only
        .address_space:  global
        .offset:         80
        .size:           8
        .value_kind:     global_buffer
    .group_segment_fixed_size: 33792
    .kernarg_segment_align: 8
    .kernarg_segment_size: 88
    .language:       OpenCL C
    .language_version:
      - 2
      - 0
    .max_flat_workgroup_size: 256
    .name:           _Z6k_prepPKfS0_S0_S0_PDF16_S1_S1_S1_S0_S0_S0_
    .private_segment_fixed_size: 0
    .sgpr_count:     22
    .sgpr_spill_count: 0
    .symbol:         _Z6k_prepPKfS0_S0_S0_PDF16_S1_S1_S1_S0_S0_S0_.kd
    .uniform_work_group_size: 1
    .uses_dynamic_stack: false
    .vgpr_count:     200
    .vgpr_spill_count: 0
    .wavefront_size: 64
  - .agpr_count:     0
    .args:
      - .actual_access:  read_only
        .address_space:  global
        .offset:         0
        .size:           8
        .value_kind:     global_buffer
      - .actual_access:  read_only
        .address_space:  global
        .offset:         8
        .size:           8
        .value_kind:     global_buffer
      - .actual_access:  read_only
        .address_space:  global
        .offset:         16
        .size:           8
        .value_kind:     global_buffer
      - .actual_access:  write_only
        .address_space:  global
        .offset:         24
        .size:           8
        .value_kind:     global_buffer
    .group_segment_fixed_size: 0
    .kernarg_segment_align: 8
    .kernarg_segment_size: 32
    .language:       OpenCL C
    .language_version:
      - 2
      - 0
    .max_flat_workgroup_size: 128
    .name:           _Z7k_finalPKfS0_S0_Pf
    .private_segment_fixed_size: 0
    .sgpr_count:     18
    .sgpr_spill_count: 0
    .symbol:         _Z7k_finalPKfS0_S0_Pf.kd
    .uniform_work_group_size: 1
    .uses_dynamic_stack: false
    .vgpr_count:     82
    .vgpr_spill_count: 0
    .wavefront_size: 64
  - .agpr_count:     0
    .args:
      - .actual_access:  read_only
        .address_space:  global
        .offset:         0
        .size:           8
        .value_kind:     global_buffer
      - .actual_access:  read_only
        .address_space:  global
        .offset:         8
        .size:           8
        .value_kind:     global_buffer
      - .actual_access:  read_only
        .address_space:  global
        .offset:         16
        .size:           8
        .value_kind:     global_buffer
      - .actual_access:  read_only
        .address_space:  global
        .offset:         24
        .size:           8
        .value_kind:     global_buffer
      - .actual_access:  read_only
        .address_space:  global
        .offset:         32
        .size:           8
        .value_kind:     global_buffer
      - .actual_access:  write_only
        .address_space:  global
        .offset:         40
        .size:           8
        .value_kind:     global_buffer
      - .actual_access:  write_only
        .address_space:  global
        .offset:         48
        .size:           8
        .value_kind:     global_buffer
      - .actual_access:  read_only
        .address_space:  global
        .offset:         56
        .size:           8
        .value_kind:     global_buffer
      - .actual_access:  read_only
        .address_space:  global
        .offset:         64
        .size:           8
        .value_kind:     global_buffer
    .group_segment_fixed_size: 33808
    .kernarg_segment_align: 8
    .kernarg_segment_size: 72
    .language:       OpenCL C
    .language_version:
      - 2
      - 0
    .max_flat_workgroup_size: 384
    .name:           _Z6k_gemmILi0EEvPKDF16_S1_PKfS3_S1_PDF16_PfS1_S5_
    .private_segment_fixed_size: 0
    .sgpr_count:     20
    .sgpr_spill_count: 0
    .symbol:         _Z6k_gemmILi0EEvPKDF16_S1_PKfS3_S1_PDF16_PfS1_S5_.kd
    .uniform_work_group_size: 1
    .uses_dynamic_stack: false
    .vgpr_count:     150
    .vgpr_spill_count: 0
    .wavefront_size: 64
  - .agpr_count:     0
    .args:
      - .actual_access:  read_only
        .address_space:  global
        .offset:         0
        .size:           8
        .value_kind:     global_buffer
      - .actual_access:  read_only
        .address_space:  global
        .offset:         8
        .size:           8
        .value_kind:     global_buffer
      - .actual_access:  read_only
        .address_space:  global
        .offset:         16
        .size:           8
        .value_kind:     global_buffer
      - .actual_access:  read_only
        .address_space:  global
        .offset:         24
        .size:           8
        .value_kind:     global_buffer
      - .actual_access:  read_only
        .address_space:  global
        .offset:         32
        .size:           8
        .value_kind:     global_buffer
      - .actual_access:  read_only
        .address_space:  global
        .offset:         40
        .size:           8
        .value_kind:     global_buffer
      - .actual_access:  read_only
        .address_space:  global
        .offset:         48
        .size:           8
        .value_kind:     global_buffer
      - .actual_access:  read_only
        .address_space:  global
        .offset:         56
        .size:           8
        .value_kind:     global_buffer
      - .actual_access:  write_only
        .address_space:  global
        .offset:         64
        .size:           8
        .value_kind:     global_buffer
    .group_segment_fixed_size: 50176
    .kernarg_segment_align: 8
    .kernarg_segment_size: 72
    .language:       OpenCL C
    .language_version:
      - 2
      - 0
    .max_flat_workgroup_size: 384
    .name:           _Z6k_gemmILi1EEvPKDF16_S1_PKfS3_S1_PDF16_PfS1_S5_
    .private_segment_fixed_size: 0
    .sgpr_count:     20
    .sgpr_spill_count: 0
    .symbol:         _Z6k_gemmILi1EEvPKDF16_S1_PKfS3_S1_PDF16_PfS1_S5_.kd
    .uniform_work_group_size: 1
    .uses_dynamic_stack: false
    .vgpr_count:     182
    .vgpr_spill_count: 0
    .wavefront_size: 64
